# conversion-in-attention: 8 units per wave, one every 6th iteration
# baseline (speedup 1.0000x reference)
; #define LAS __attribute__((address_space(3)))
; __device__ __forceinline__ void convert_experts(Frame& F, int lo, int hi) {
;     const int gw = F.vcu * 8 + F.wave, NGW = F.G * 8;
;     LAS unsigned char* scr = F.lds + F.wave * 16384;
;     unsigned char* W1t = WSP(F, WS_W1T, unsigned char); unsigned char* W2t = WSP(F, WS_W2T, unsigned char);
;     const float* weg = F.a->in[I_WEG]; const float* weu = F.a->in[I_WEU]; const float* wed = F.a->in[I_WED];
;     const float* wsg = F.a->in[I_WSG]; const float* wsu = F.a->in[I_WSU]; const float* wsd = F.a->in[I_WSD];
;     ...
;     constexpr int NPAIRS = CONV_ITEMS / 2;
;     (void)lo; (void)hi;
;     ...
;     if (gw < NPAIRS) {
;         const int ns = 2 * ((NPAIRS - gw + NGW - 1) / NGW);
;         int sq = 0, r = CONV_RIDX(0);
;         TItem tc, tn; CONV_DESC(r, tc); tn = tc;
;         int p = 0; bool first = true;
;         titem_issue(tc, F.lane, scr);
;         for (;;) {
;             const bool more = sq + 1 < ns; const int rn = more ? CONV_RIDX(sq + 1) : r;
;             if (more) { CONV_DESC(rn, tn); titem_issue(tn, F.lane, scr + (p ^ 1) * 8192); }
;             if (!more) asm volatile("s_waitcnt vmcnt(0)" ::: "memory");
;             else if (first) asm volatile("s_waitcnt vmcnt(8)" ::: "memory");
;             else asm volatile("s_waitcnt vmcnt(12)" ::: "memory");
;             titem_finish(tc, F.lane, scr + p * 8192);
;             asm volatile("s_waitcnt lgkmcnt(0)" ::: "memory");
;             if (!more) break;
;             tc = tn; r = rn; ++sq; p ^= 1; first = false;
;         }
;     }
.Lcv1_vcu:
	s_lshl_b32 s11, s11, 3
	s_add_u32 s89, s11, s9
	s_lshl_b32 s71, s8, 3
	s_mul_i32 s10, s71, 8
	s_add_u32 s89, s89, s10
	s_mov_b32 s69, s89
	s_add_u32 s86, s84, 0x9180000
	s_addc_u32 s87, s85, 0
	s_add_u32 s84, s84, 0x1100000
	s_addc_u32 s85, s85, 0
	s_mov_b32 s90, 0xc2b8aa3b
	s_cmp_ge_u32 s89, 49344
	s_cbranch_scc1 .Lcv1_done
	s_cmp_lt_u32 s69, 49344
	s_cbranch_scc0 .Lcv1_dummyA1
	s_lshr_b32 s10, s69, 6
	s_and_b32 s12, s69, 63
	s_mul_hi_u32 s14, s10, 0xaaaaaaab
	s_lshr_b32 s14, s14, 1
	s_mul_i32 s11, s14, 3
	s_sub_u32 s11, s10, s11
	s_cmp_lt_u32 s14, 256
	s_cselect_b32 s10, s14, 0
	s_cselect_b64 s[44:45], -1, 0
	s_lshl_b32 s10, s10, 20
	s_cmp_eq_u32 s11, 2
	s_cbranch_scc1 .Lcv1_downA1
	s_cmp_eq_u32 s11, 0
	s_cselect_b64 s[4:5], s[72:73], s[74:75]
	s_cselect_b64 s[38:39], s[78:79], s[80:81]
	s_mov_b32 s94, 0xc3317218
	s_cselect_b32 s94, s90, s94
	s_cmp_lg_u64 s[44:45], 0
	s_cselect_b64 s[4:5], s[4:5], s[38:39]
	s_lshr_b32 s38, s12, 3
	s_and_b32 s39, s12, 7
	s_lshl_b32 s8, s38, 17
	s_add_u32 s10, s10, s8
	s_lshl_b32 s8, s39, 7
	s_add_u32 s10, s10, s8
	s_add_u32 s4, s4, s10
	s_addc_u32 s5, s5, 0
	s_lshl_b32 s14, s14, 19
	s_lshr_b32 s8, s39, 2
	s_lshl_b32 s8, s8, 18
	s_add_u32 s14, s14, s8
	s_and_b32 s8, s39, 3
	s_lshl_b32 s8, s8, 15
	s_add_u32 s14, s14, s8
	s_lshl_b32 s8, s11, 17
	s_add_u32 s14, s14, s8
	s_lshl_b32 s8, s38, 7
	s_add_u32 s14, s14, s8
	s_add_u32 s92, s84, s14
	s_addc_u32 s93, s85, 0
	s_movk_i32 s25, 0x400
	s_movk_i32 s27, 0x1000
	s_movk_i32 s8, 0x400
	s_movk_i32 s9, 0x4000
	s_branch .Lcv1_goA1

; #define LAS __attribute__((address_space(3)))
; __device__ __forceinline__ void convert_experts(Frame& F, int lo, int hi) {
;     const int gw = F.vcu * 8 + F.wave, NGW = F.G * 8;
;     LAS unsigned char* scr = F.lds + F.wave * 16384;
;     unsigned char* W1t = WSP(F, WS_W1T, unsigned char); unsigned char* W2t = WSP(F, WS_W2T, unsigned char);
;     const float* weg = F.a->in[I_WEG]; const float* weu = F.a->in[I_WEU]; const float* wed = F.a->in[I_WED];
;     const float* wsg = F.a->in[I_WSG]; const float* wsu = F.a->in[I_WSU]; const float* wsd = F.a->in[I_WSD];
;     ...
;     constexpr int NPAIRS = CONV_ITEMS / 2;
;     (void)lo; (void)hi;
.Lcva_vcu:
	s_lshr_b32 s99, s99, 6
	s_lshl_b32 s101, s101, 3
	s_add_u32 s89, s101, s99
	s_movk_i32 s90, 8
	s_lshr_b32 s32, s89, 3
	s_and_b32 s32, s32, 3
	s_cmp_ge_u32 s32, 6
	s_cselect_b32 s99, 6, 0
	s_sub_u32 s32, s32, s99
	s_mov_b32 s95, 0
	s_waitcnt vmcnt(0)
	s_branch .LBB0_304

; #define LAS __attribute__((address_space(3)))
; __device__ __forceinline__ void lds_barrier() { asm volatile("s_waitcnt lgkmcnt(0)\n\ts_barrier" ::: "memory"); }
; __device__ __forceinline__ void phase_attn(Frame& F) {
;     ...
;         lds_barrier();
;         LAS unsigned char* kb = F.lds + buf * ABUF;
;         const bf16x8 q0 = qn0, q1 = qn1;
;         {
;             LAS unsigned char* ob = F.lds + (buf ^ 1) * ABUF;
; #pragma unroll
;             for (int jj = 0; jj < 4; ++jj) { const int ch = tid + 512 * jj, row = ch >> 3, c16 = ch & 7;
;                 *(LAS u32x4*)(ob + row * ATT_ROWB + c16 * 16) = kr[jj]; *(LAS u32x4*)(ob + ATT_VOFF + row * ATT_ROWB + c16 * 16) = vr[jj]; }
;         }
;         const AttnUnit nu = un;
;         un = attn_decode(x8 * PER_X + (jl + 2 * G8 < jlast ? jl + 2 * G8 : jlast)); attn_issue(qkv, un, tid, kr, vr);
;         { const char* qb = (const char*)qkv + (((size_t)nu.b * SEQ + nu.r) * NPROJ + nu.h * 64) * 2; const unsigned qo = __umul24((unsigned)(128 * nu.n + ql), (unsigned)nu.d * (NPROJ * 2)) + 16u * fq;
;           qn0 = *(const bf16x8*)(qb + qo); qn1 = *(const bf16x8*)(qb + qo + 64); }
;         const unsigned qrow = __umul24((unsigned)(128 * cu.n + ql), (unsigned)cu.d);
;         const float c1 = 0.125f * LOG2E;
;         const float nc2 = -__builtin_amdgcn_exp2f(-(float)(cu.h + 1)) * (float)cu.d * LOG2E;
;         const bool first = cu.n == 0;
;         f32x4 St[9];
;         const f32x4 eb = (f32x4){ef[0], ef[1], ef[2], ef[3]} * nc2;
;         float mx = -INFINITY;
;         bf16x8 kf[9][2];
; #pragma unroll
;         for (int T = 0; T < 9; ++T) { LAS unsigned char* ka = kb + (16 * (w + T) + fr) * ATT_ROWB + fq * 16; kf[T][0] = *(LAS bf16x8*)ka; kf[T][1] = *(LAS bf16x8*)(ka + 64); }
.Lcva_wd:
	v_mov_b64_e32 v[48:49], v[4:5]
	v_mov_b64_e32 v[46:47], v[2:3]
	v_mov_b64_e32 v[44:45], v[8:9]
	v_mov_b64_e32 v[42:43], v[6:7]
	s_lshl_b32 s65, 1, s35
	s_waitcnt lgkmcnt(0)
	s_barrier
	s_add_i32 s37, s30, 1
	v_cvt_f32_u32_e32 v54, s37
	v_cvt_f32_u32_e32 v55, s65
	v_add_u32_e32 v110, s85, v82
	v_add_u32_e32 v58, v110, v90
	v_exp_f32_e64 v54, -v54
	v_add_u32_e32 v66, v110, v91
	v_add_u32_e32 v74, v110, v92
	v_add_u32_e32 v111, v110, v93
	v_mul_f32_e32 v79, v55, v54
	ds_read_b128 v[54:57], v58
	ds_read_b128 v[58:61], v58 offset:64
	ds_read_b128 v[62:65], v66
	ds_read_b128 v[66:69], v66 offset:64
	ds_read_b128 v[70:73], v74
	ds_read_b128 v[74:77], v74 offset:64
	ds_read_b128 v[112:115], v111
	ds_read_b128 v[116:119], v111 offset:64
	v_add_u32_e32 v111, v110, v94
	ds_read_b128 v[120:123], v111
	ds_read_b128 v[124:127], v111 offset:64
	v_add_u32_e32 v111, v110, v95
	ds_read_b128 v[128:131], v111
	ds_read_b128 v[132:135], v111 offset:64
	v_add_u32_e32 v111, v110, v96
	ds_read_b128 v[136:139], v111
	ds_read_b128 v[140:143], v111 offset:64
	v_add_u32_e32 v111, v110, v97
	v_add_u32_e32 v110, v110, v98
	ds_read_b128 v[144:147], v111
	ds_read_b128 v[148:151], v111 offset:64
	ds_read_b128 v[152:155], v110
	ds_read_b128 v[156:159], v110 offset:64
	s_sub_u32 s32, s32, 1
	s_cmp_lt_i32 s32, 0
	s_cbranch_scc0 .Lcva_none_l
	s_mov_b32 s32, 5
	s_cmp_eq_u32 s90, 0
	s_cbranch_scc1 .Lcva_none_l
	s_sub_u32 s90, s90, 1
	s_lshr_b32 s98, s89, 6
	s_and_b32 s99, s89, 63
	s_mul_hi_u32 s100, s98, 0xaaaaaaab
	s_lshr_b32 s100, s100, 1
	s_mul_i32 s101, s100, 3
	s_sub_u32 s101, s98, s101
	s_cmp_lt_u32 s100, 256
	s_cselect_b32 s98, 0, 3
	s_cselect_b32 s95, s100, 0
	s_add_u32 s98, s98, s101
	s_lshl_b32 s98, s98, 1
	v_readlane_b32 s96, v253, s98
	s_add_u32 s98, s98, 1
	v_readlane_b32 s97, v253, s98
	s_lshl_b32 s95, s95, 20
	s_nop 3
	s_add_u32 s96, s96, s95
	s_addc_u32 s97, s97, 0
	s_cmp_eq_u32 s101, 2
	s_cbranch_scc1 .Lcva_down_l
	s_lshr_b32 s95, s99, 3
	s_and_b32 s99, s99, 7
	s_lshl_b32 s98, s95, 17
	s_add_u32 s96, s96, s98
	s_addc_u32 s97, s97, 0
	s_lshl_b32 s98, s99, 7
	s_add_u32 s96, s96, s98
	s_addc_u32 s97, s97, 0
	s_lshl_b32 s100, s100, 19
	s_lshr_b32 s98, s99, 2
	s_lshl_b32 s98, s98, 18
	s_add_u32 s100, s100, s98
	s_and_b32 s98, s99, 3
	s_lshl_b32 s98, s98, 15
	s_add_u32 s100, s100, s98
	s_lshl_b32 s98, s101, 17
	s_add_u32 s100, s100, s98
	s_lshl_b32 s98, s95, 7
	s_add_u32 s100, s100, s98
	v_readlane_b32 s92, v253, 12
	v_readlane_b32 s93, v253, 13
	s_mov_b32 s94, 0xc3317218
	s_cmp_eq_u32 s101, 0
	s_cselect_b32 s94, 0xc2b8aa3b, s94
	s_nop 3
	s_add_u32 s92, s92, s100
	s_addc_u32 s93, s93, 0
	s_movk_i32 s95, 0x400
	s_movk_i32 s98, 0x400
	s_branch .Lcva_go_l
